# code placement: P8 expert up-projection K-loop moved by +32 bytes (pad in the once-per-phase guard block), P9 and later code kept at the same address modulo 64
# speedup vs baseline: 1.0131x; 1.0046x over previous
.LBB0_1167:
	s_nop 0
	s_nop 0
	s_nop 0
	s_nop 0
	s_nop 0
	s_nop 0
	s_nop 0
	s_nop 0
	v_readlane_b32 s2, v251, 14
	v_readlane_b32 s3, v251, 15
	s_cmp_lt_i32 s2, 9
	s_cselect_b64 s[2:3], -1, 0
	s_and_b64 s[0:1], s[2:3], s[0:1]
	s_andn2_b64 vcc, exec, s[0:1]
	s_cbranch_vccnz .LBB0_1200
	v_readlane_b32 s0, v251, 16
	v_mbcnt_lo_u32_b32 v0, -1, 0
	v_mbcnt_hi_u32_b32 v0, -1, v0
	s_andn2_b32 s0, s0, 63
	s_nop 0
	v_add_u32_e32 v0, s0, v0
	v_cmp_gt_i32_e32 vcc, 33, v0
	s_waitcnt lgkmcnt(0)
	v_lshl_add_u32 v2, v0, 2, 0
	s_and_saveexec_b64 s[4:5], vcc
	s_cbranch_execz .LBB0_1170
	v_readlane_b32 s8, v251, 10
	v_ashrrev_i32_e32 v1, 31, v0
	v_readlane_b32 s10, v251, 12
	v_readlane_b32 s11, v251, 13
	v_add_u32_e32 v3, 0x24240, v2
	v_readlane_b32 s9, v251, 11
	v_lshl_add_u64 v[4:5], v[0:1], 2, s[10:11]
	v_add_co_u32_e32 v4, vcc, 0x66280000, v4
	s_nop 1
	v_addc_co_u32_e32 v5, vcc, 0, v5, vcc
	global_load_dword v1, v[4:5], off
	s_waitcnt vmcnt(0)
	ds_write_b32 v3, v1

.LBB0_1252:
	s_nop 0
	s_nop 0
	s_nop 0
	s_nop 0
	s_nop 0
	s_nop 0
	s_nop 0
	s_nop 0
	v_readlane_b32 s2, v251, 14
	v_readlane_b32 s3, v251, 15
	s_cmp_lt_i32 s2, 10
	s_cselect_b64 s[2:3], -1, 0
	s_and_b64 s[0:1], s[2:3], s[0:1]
	s_andn2_b64 vcc, exec, s[0:1]
	s_cbranch_vccnz .LBB0_1293
	v_readlane_b32 s0, v251, 16
	v_mbcnt_lo_u32_b32 v0, -1, 0
	v_mbcnt_hi_u32_b32 v0, -1, v0
	s_and_b32 s6, s0, 0xffffffc0
	v_add_u32_e32 v0, s6, v0
	v_cmp_gt_i32_e32 vcc, 33, v0
	s_waitcnt lgkmcnt(0)
	v_lshl_add_u32 v2, v0, 2, 0
	s_and_saveexec_b64 s[0:1], vcc
	s_cbranch_execz .LBB0_1255
	v_readlane_b32 s8, v251, 10
	v_ashrrev_i32_e32 v1, 31, v0
	v_readlane_b32 s10, v251, 12
	v_readlane_b32 s11, v251, 13
	v_add_u32_e32 v3, 0x24240, v2
	v_readlane_b32 s9, v251, 11
	v_lshl_add_u64 v[4:5], v[0:1], 2, s[10:11]
	v_add_co_u32_e32 v4, vcc, 0x66280000, v4
	s_nop 1
	v_addc_co_u32_e32 v5, vcc, 0, v5, vcc
	global_load_dword v1, v[4:5], off
	s_waitcnt vmcnt(0)
	ds_write_b32 v3, v1
